# v22: v10 + phase-5 weight-conversion filler visits tiles n-fastest inside each expert (adjacent workers read adjacent 512B pieces of the same 64 source rows)
# speedup vs baseline: 1.0004x; 1.0004x over previous
.LBB0_715:
	s_abs_i32 s0, s33
	v_cvt_f32_u32_e32 v2, s0
	s_sub_i32 s1, 0, s0
	v_rcp_iflag_f32_e32 v2, v2
	s_nop 0
	v_mul_f32_e32 v2, 0x4f7ffffe, v2
	v_cvt_u32_f32_e32 v2, v2
	s_nop 0
	v_readfirstlane_b32 s3, v2
	s_mul_i32 s1, s1, s3
	s_mul_hi_u32 s1, s3, s1
	s_add_i32 s3, s3, s1
	s_mul_hi_u32 s1, s3, 0x410
	s_mul_i32 s1, s1, s0
	s_sub_i32 s1, 0x410, s1
	s_sub_i32 s3, s1, s0
	s_cmp_ge_u32 s1, s0
	s_cselect_b32 s1, s3, s1
	s_sub_i32 s3, s1, s0
	s_cmp_ge_u32 s1, s0
	s_cselect_b32 s0, s3, s1
	s_sub_i32 s3, s33, s0
	s_cmp_gt_i32 s3, 0
	s_cselect_b64 s[4:5], -1, 0
	s_and_b64 s[6:7], s[4:5], exec
	s_cselect_b32 s0, s0, 0
	s_sub_i32 s6, s2, s0
	s_cmp_lt_i32 s6, 0
	s_cbranch_scc1 .LBB0_729
	s_and_b64 s[4:5], s[4:5], exec
	s_cselect_b32 s3, s3, s33
	s_abs_i32 s0, s3
	v_cvt_f32_u32_e32 v2, s0
	s_ashr_i32 s1, s6, 31
	s_abs_i32 s4, s6
	s_sub_i32 s5, 0, s0
	v_rcp_iflag_f32_e32 v2, v2
	s_nop 0
	v_mul_f32_e32 v2, 0x4f7ffffe, v2
	v_cvt_u32_f32_e32 v2, v2
	s_nop 0
	v_readfirstlane_b32 s6, v2
	s_mul_i32 s5, s5, s6
	s_mul_hi_u32 s5, s6, s5
	s_add_i32 s6, s6, s5
	s_mul_hi_u32 s5, s4, s6
	s_mul_i32 s5, s5, s0
	s_sub_i32 s4, s4, s5
	s_sub_i32 s5, s4, s0
	s_cmp_ge_u32 s4, s0
	s_cselect_b32 s4, s5, s4
	s_sub_i32 s5, s4, s0
	s_cmp_ge_u32 s4, s0
	s_cselect_b32 s4, s5, s4
	s_xor_b32 s4, s4, s1
	s_sub_i32 s1, s4, s1
	s_add_i32 s1, s1, s3
	s_ashr_i32 s4, s1, 31
	s_abs_i32 s1, s1
	s_mul_hi_u32 s5, s1, s6
	s_mul_i32 s5, s5, s0
	s_sub_i32 s1, s1, s5
	s_sub_i32 s5, s1, s0
	s_cmp_ge_u32 s1, s0
	s_cselect_b32 s1, s5, s1
	s_sub_i32 s5, s1, s0
	s_cmp_ge_u32 s1, s0
	s_cselect_b32 s0, s5, s1
	s_xor_b32 s0, s0, s4
	s_waitcnt lgkmcnt(0)
	s_sub_i32 s14, s0, s4
	s_cmpk_gt_i32 s14, 0x1fff
	s_cbranch_scc1 .LBB0_729
	s_and_b32 s101, s14, 0xffffff00
	s_and_b32 s100, s14, 7
	s_lshl_b32 s100, s100, 5
	s_or_b32 s101, s101, s100
	s_bfe_u32 s100, s14, 0x50003
	s_or_b32 s101, s101, s100
	s_ashr_i32 s0, s101, 31
	s_lshr_b32 s1, s0, 27
	s_lshr_b32 s0, s0, 24
	s_add_i32 s1, s101, s1
	s_add_i32 s0, s101, s0
	s_lshl_b32 s5, s1, 2
	s_ashr_i32 s10, s0, 8
	s_bfe_i32 s0, s1, 0x1001d
	s_and_b32 s5, s5, 0xffffff80
	s_lshr_b32 s0, s0, 22
	s_load_dwordx4 s[16:19], s[74:75], 0x120
	s_add_i32 s0, s5, s0
	s_and_b32 s0, s0, 0xfffffc00
	v_lshlrev_b32_e32 v2, 3, v0
	s_sub_i32 s0, s5, s0
	v_and_b32_e32 v44, 56, v2
	v_or_b32_e32 v3, s0, v44
	s_and_b32 s4, s1, 0x3ffffe0
	v_and_b32_e32 v4, 2, v0
	v_ashrrev_i32_e32 v3, 1, v3
	v_and_b32_e32 v45, 8, v2
	s_movk_i32 s0, 0xffd0
	s_sub_i32 s4, s101, s4
	v_and_or_b32 v18, v3, s0, v45
	s_waitcnt lgkmcnt(0)
	v_mov_b32_e32 v2, s19
	v_mov_b32_e32 v3, s17
	v_cmp_eq_u32_e64 s[6:7], 0, v4
	v_lshl_or_b32 v36, s4, 6, v1
	s_movk_i32 s1, 0x7ff
	s_ashr_i32 s11, s10, 31
	v_mov_b32_e32 v37, 0
	v_cndmask_b32_e64 v35, v2, v3, s[6:7]
	v_mov_b32_e32 v2, s18
	v_mov_b32_e32 v3, s16
	v_cmp_lt_u32_e32 vcc, s1, v36
	s_movk_i32 s1, 0x800
	v_cndmask_b32_e64 v34, v2, v3, s[6:7]
	s_lshl_b64 s[6:7], s[10:11], 22
	s_movk_i32 s0, 0x200
	v_mov_b32_e32 v4, v37
	v_mov_b32_e32 v5, v37
	v_cmp_gt_u32_e64 s[4:5], s1, v36
	v_lshl_add_u64 v[20:21], v[34:35], 0, s[6:7]
	v_cmp_gt_i32_e64 s[6:7], s0, v18
	v_mov_b32_e32 v2, v37
	v_mov_b32_e32 v3, v37
	v_mov_b64_e32 v[8:9], v[4:5]
	s_and_b64 s[6:7], s[4:5], s[6:7]
	v_ashrrev_i32_e32 v19, 31, v18
	v_lshlrev_b64 v[22:23], 11, v[36:37]
	v_mov_b64_e32 v[6:7], v[2:3]
	s_and_saveexec_b64 s[4:5], s[6:7]
	s_cbranch_execz .LBB0_719
	v_lshl_add_u64 v[2:3], v[20:21], 0, v[22:23]
	v_lshl_add_u64 v[10:11], v[18:19], 2, v[2:3]
	global_load_dwordx4 v[6:9], v[10:11], off offset:16
	global_load_dwordx4 v[2:5], v[10:11], off

.LBB0_721:
	s_or_b64 exec, exec, s[4:5]
	s_add_u32 s10, s54, 0x39800000
	s_addc_u32 s11, s55, 0
	v_lshl_add_u32 v10, v44, 2, 0
	v_mul_u32_u24_e32 v18, 0x204, v1
	v_lshl_add_u32 v19, v188, 2, 0
	v_mul_u32_u24_e32 v20, 0x204, v146
	s_lshl_b32 s17, s3, 6
	v_mov_b32_e32 v39, 0
	s_lshl_b32 s16, s14, 6
	v_or_b32_e32 v1, s17, v1
	v_and_b32_e32 v120, 63, v1
	s_movk_i32 s18, 0x7ff
	s_movk_i32 s19, 0x800
	s_movk_i32 s20, 0xffd0
	s_movk_i32 s21, 0x200
	v_add_u32_e32 v36, v10, v18
	v_add_u32_e32 v46, v19, v20
	v_lshlrev_b32_e32 v10, 1, v146
	s_branch .LBB0_724

.LBB0_723:
	s_waitcnt vmcnt(0)
	ds_write2_b32 v36, v2, v3 offset1:1
	ds_write2_b32 v36, v4, v5 offset0:2 offset1:3
	ds_write2_b32 v36, v6, v7 offset0:4 offset1:5
	ds_write2_b32 v36, v8, v9 offset0:6 offset1:7
	ds_write2_b32 v36, v37, v11 offset0:64 offset1:65
	ds_write2_b32 v36, v12, v13 offset0:66 offset1:67
	ds_write2_b32 v36, v14, v15 offset0:68 offset1:69
	ds_write2_b32 v36, v16, v17 offset0:70 offset1:71
	v_add_u32_e32 v6, 0x800, v46
	s_waitcnt lgkmcnt(0)
	s_barrier
	v_add_u32_e32 v4, 0x400, v46
	ds_read2_b32 v[8:9], v6 offset0:4 offset1:133
	v_add_u32_e32 v6, 0xc00, v46
	ds_read2_b32 v[2:3], v46 offset1:129
	ds_read2_b32 v[4:5], v4 offset0:2 offset1:131
	ds_read2_b32 v[12:13], v6 offset0:6 offset1:135
	s_and_b32 s101, s14, 0xffffff00
	s_and_b32 s100, s14, 7
	s_lshl_b32 s100, s100, 5
	s_or_b32 s101, s101, s100
	s_bfe_u32 s100, s14, 0x50003
	s_or_b32 s101, s101, s100
	s_lshl_b32 s100, s101, 6
	s_ashr_i32 s0, s101, 31
	s_lshr_b32 s0, s0, 27
	v_add_u32_e32 v11, 0x1400, v46
	s_add_i32 s0, s101, s0
	ds_read2_b32 v[14:15], v11 offset0:10 offset1:139
	v_add_u32_e32 v11, 0x1800, v46
	s_ashr_i32 s0, s0, 5
	v_add_u32_e32 v6, 0x1000, v46
	ds_read2_b32 v[16:17], v11 offset0:12 offset1:141
	v_add_u32_e32 v11, 0x1c00, v46
	ds_read2_b32 v[6:7], v6 offset0:8 offset1:137
	ds_read2_b32 v[40:41], v11 offset0:14 offset1:143
	s_waitcnt lgkmcnt(6)
	v_cvt_pk_bf16_f32 v2, v2, v3
	s_waitcnt lgkmcnt(5)
	v_cvt_pk_bf16_f32 v3, v4, v5
	s_waitcnt lgkmcnt(4)
	v_cvt_pk_bf16_f32 v5, v12, v13
	v_lshl_or_b32 v12, s0, 7, v188
	v_ashrrev_i32_e32 v13, 31, v12
	s_lshl_b32 s0, s0, 11
	v_lshlrev_b64 v[12:13], 12, v[12:13]
	s_sub_i32 s4, s100, s0
	v_lshl_add_u64 v[12:13], s[10:11], 0, v[12:13]
	s_ashr_i32 s5, s4, 31
	v_lshl_add_u64 v[12:13], s[4:5], 1, v[12:13]
	v_mov_b32_e32 v11, v39
	s_waitcnt lgkmcnt(1)
	v_cvt_pk_bf16_f32 v6, v6, v7
	v_cvt_pk_bf16_f32 v7, v14, v15
	v_cvt_pk_bf16_f32 v4, v8, v9
	v_cvt_pk_bf16_f32 v8, v16, v17
	s_waitcnt lgkmcnt(0)
	v_cvt_pk_bf16_f32 v9, v40, v41
	v_lshl_add_u64 v[12:13], v[12:13], 0, v[10:11]
	global_store_dwordx4 v[12:13], v[2:5], off
	global_store_dwordx4 v[12:13], v[6:9], off offset:16
	s_add_i32 s16, s16, s17
	v_mov_b64_e32 v[2:3], v[18:19]
	v_mov_b64_e32 v[6:7], v[22:23]
	s_andn2_b64 vcc, exec, s[12:13]
	v_mov_b64_e32 v[8:9], v[24:25]
	v_mov_b64_e32 v[4:5], v[20:21]
	s_mov_b32 s14, s22
	v_mov_b32_e32 v14, v30
	v_mov_b32_e32 v15, v31
	v_mov_b32_e32 v16, v32
	v_mov_b32_e32 v17, v33
	v_mov_b32_e32 v37, v26
	v_mov_b32_e32 v11, v27
	v_mov_b32_e32 v12, v28
	v_mov_b32_e32 v13, v29
	s_barrier
	s_cbranch_vccz .LBB0_729
.LBB0_724:
	s_add_i32 s22, s14, s3
	s_cmpk_gt_i32 s22, 0x1fff
	s_cselect_b64 s[12:13], -1, 0
	s_and_b64 vcc, exec, s[12:13]
	s_cbranch_vccnz .LBB0_723
	s_and_b32 s99, s22, 0xffffff00
	s_and_b32 s98, s22, 7
	s_lshl_b32 s98, s98, 5
	s_or_b32 s99, s99, s98
	s_bfe_u32 s98, s22, 0x50003
	s_or_b32 s99, s99, s98
	s_lshl_b32 s98, s99, 6
	s_ashr_i32 s0, s99, 31
	s_lshr_b32 s1, s0, 27
	s_add_i32 s1, s99, s1
	s_lshr_b32 s0, s0, 24
	s_ashr_i32 s1, s1, 5
	s_add_i32 s0, s99, s0
	s_ashr_i32 s6, s0, 8
	s_bfe_i32 s0, s1, 0x10018
	s_lshl_b32 s4, s1, 7
	s_lshr_b32 s0, s0, 22
	s_add_i32 s0, s4, s0
	s_and_b32 s0, s0, 0xfffffc00
	s_sub_i32 s0, s4, s0
	v_add_u32_e32 v18, s98, v120
	s_lshl_b32 s1, s1, 11
	v_subrev_u32_e32 v38, s1, v18
	v_or_b32_e32 v18, s0, v44
	s_ashr_i32 s7, s6, 31
	v_ashrrev_i32_e32 v18, 1, v18
	s_lshl_b64 s[6:7], s[6:7], 22
	v_and_or_b32 v40, v18, s20, v45
	v_lshl_add_u64 v[22:23], v[34:35], 0, s[6:7]
	v_mov_b32_e32 v20, v39
	v_mov_b32_e32 v21, v39
	v_lshlrev_b64 v[24:25], 11, v[38:39]
	v_cmp_gt_u32_e64 s[4:5], s19, v38
	v_cmp_gt_i32_e64 s[6:7], s21, v40
	v_mov_b32_e32 v18, v39
	v_mov_b32_e32 v19, v39
	v_lshl_add_u64 v[42:43], v[22:23], 0, v[24:25]
	v_mov_b64_e32 v[24:25], v[20:21]
	v_cmp_lt_u32_e32 vcc, s18, v38
	s_and_b64 s[6:7], s[4:5], s[6:7]
	v_ashrrev_i32_e32 v41, 31, v40
	v_mov_b64_e32 v[22:23], v[18:19]
	s_and_saveexec_b64 s[4:5], s[6:7]
	s_cbranch_execz .LBB0_727
	v_lshl_add_u64 v[26:27], v[40:41], 2, v[42:43]
	global_load_dwordx4 v[22:25], v[26:27], off offset:16
	global_load_dwordx4 v[18:21], v[26:27], off
